# v30 with exact vmcnt in the second halves of the P3 loops (prefetch for tile j+3 no longer drained; last-iteration drain on the skip path)
# baseline (speedup 1.0000x reference)
; #define SWAIT() do { if constexpr (MODE == 1) asm volatile("s_waitcnt vmcnt(3)" ::: "memory"); else asm volatile("s_waitcnt vmcnt(4)" ::: "memory"); } while (0)
; #define RESC(a) do { if (__any((a) < 1.f)) { if (hi == 0) al_l[r32] = (a); asm volatile("s_waitcnt lgkmcnt(0)" ::: "memory"); \
;     _Pragma("unroll") for (int d = 0; d < 4; ++d) _Pragma("unroll") for (int r = 0; r < 16; ++r) o[d][r] *= al_l[crow(r, hi)]; } } while (0)
; template <int MODE>
; __device__ __forceinline__ void partialSM(f32x16& p0, f32x16& p1, float& m_reg, float& mn, float& alpha) {
;     constexpr float SCALE = Cfg<MODE>::SCALE, C = SCALE * 1.4426950408889634f;
;     float pmax = p0[0];
; #pragma unroll
;     for (int r = 1; r < 16; ++r) pmax = fmaxf(pmax, p0[r]);
; #pragma unroll
;     for (int r = 0; r < 16; ++r) pmax = fmaxf(pmax, p1[r]);
;     { auto rr = __builtin_amdgcn_permlane32_swap(__float_as_uint(pmax), __float_as_uint(pmax), false, false);
;       pmax = fmaxf(__uint_as_float(rr[0]), __uint_as_float(rr[1])); }
;     if (__builtin_expect(__all(pmax - m_reg <= THR / SCALE), 1)) { mn = m_reg; alpha = 1.f; }
;     else { mn = fmaxf(m_reg, pmax); alpha = __builtin_amdgcn_exp2f((m_reg - mn) * C); m_reg = mn; }
;     const float mnC = -mn * C;
; #pragma unroll
;     for (int r = 0; r < 16; ++r) p0[r] = fmaf(p0[r], C, mnC);
; #pragma unroll
;     for (int r = 0; r < 16; ++r) p1[r] = fmaf(p1[r], C, mnC);
; #pragma unroll
;     for (int r = 0; r < 16; ++r) p0[r] = __builtin_amdgcn_exp2f(p0[r]);
; }
; template <int MODE>
; __device__ __forceinline__ void attn_pass(const bf16_t* __restrict__ Qb, const bf16_t* __restrict__ Kh, const bf16_t* __restrict__ Vh, const int NT, const int kr0, const int g4, const int map,
;                                           LAS unsigned char* lds, f32x16 (&o)[4]) {
;     ...
;         pv_d0(o, vb0 + SHM_V, pa0, pa1, pa2, pa3); partialSM<MODE>(pA0, pA1, m_reg, mnA, alA);
;         __syncthreads(); SWAIT(); SWRITE(1, SO);
;         RESC(alA); __syncthreads();
.LBB0_418:
	ds_read_b64_tr_b16 v[200:201], v173 offset:0
	ds_read_b64_tr_b16 v[202:203], v173 offset:0x800
	ds_read_b64_tr_b16 v[230:231], v173 offset:0x1000
	ds_read_b64_tr_b16 v[232:233], v173 offset:0x1800
	ds_read_b64_tr_b16 v[234:235], v173 offset:0x2000
	ds_read_b64_tr_b16 v[236:237], v173 offset:0x2800
	ds_read_b64_tr_b16 v[238:239], v173 offset:0x3000
	ds_read_b64_tr_b16 v[240:241], v173 offset:0x3800
	s_waitcnt lgkmcnt(0)
	s_nop 0
	v_mfma_f32_32x32x16_bf16 v[2:17], v[138:141], v[200:203], v[2:17]
	ds_read_b64_tr_b16 v[200:201], v173 offset:0x200
	ds_read_b64_tr_b16 v[202:203], v173 offset:0xa00
	v_mfma_f32_32x32x16_bf16 v[2:17], v[142:145], v[230:233], v[2:17]
	ds_read_b64_tr_b16 v[230:231], v173 offset:0x1200
	ds_read_b64_tr_b16 v[232:233], v173 offset:0x1a00
	v_mfma_f32_32x32x16_bf16 v[2:17], v[150:153], v[234:237], v[2:17]
	ds_read_b64_tr_b16 v[234:235], v173 offset:0x2200
	ds_read_b64_tr_b16 v[236:237], v173 offset:0x2a00
	ds_read_b64_tr_b16 v[242:243], v173 offset:0x3200
	ds_read_b64_tr_b16 v[244:245], v173 offset:0x3a00
	s_waitcnt lgkmcnt(0)
	v_mfma_f32_32x32x16_bf16 v[2:17], v[146:149], v[238:241], v[2:17]
	v_mfma_f32_32x32x16_bf16 v[50:65], v[138:141], v[200:203], v[50:65]
	ds_read_b64_tr_b16 v[200:201], v173 offset:0x400
	ds_read_b64_tr_b16 v[202:203], v173 offset:0xc00
	v_mfma_f32_32x32x16_bf16 v[50:65], v[142:145], v[230:233], v[50:65]
	ds_read_b64_tr_b16 v[230:231], v173 offset:0x1400
	ds_read_b64_tr_b16 v[232:233], v173 offset:0x1c00
	v_mfma_f32_32x32x16_bf16 v[50:65], v[150:153], v[234:237], v[50:65]
	ds_read_b64_tr_b16 v[234:235], v173 offset:0x2400
	ds_read_b64_tr_b16 v[236:237], v173 offset:0x2c00
	ds_read_b64_tr_b16 v[238:239], v173 offset:0x3400
	ds_read_b64_tr_b16 v[240:241], v173 offset:0x3c00
	s_waitcnt lgkmcnt(0)
	v_mfma_f32_32x32x16_bf16 v[50:65], v[146:149], v[242:245], v[50:65]
	v_mfma_f32_32x32x16_bf16 v[34:49], v[138:141], v[200:203], v[34:49]
	ds_read_b64_tr_b16 v[200:201], v173 offset:0x600
	ds_read_b64_tr_b16 v[202:203], v173 offset:0xe00
	v_mfma_f32_32x32x16_bf16 v[34:49], v[142:145], v[230:233], v[34:49]
	ds_read_b64_tr_b16 v[230:231], v173 offset:0x1600
	ds_read_b64_tr_b16 v[232:233], v173 offset:0x1e00
	v_mfma_f32_32x32x16_bf16 v[34:49], v[150:153], v[234:237], v[34:49]
	ds_read_b64_tr_b16 v[234:235], v173 offset:0x2600
	ds_read_b64_tr_b16 v[236:237], v173 offset:0x2e00
	ds_read_b64_tr_b16 v[242:243], v173 offset:0x3600
	ds_read_b64_tr_b16 v[244:245], v173 offset:0x3e00
	s_waitcnt lgkmcnt(0)
	v_mfma_f32_32x32x16_bf16 v[34:49], v[146:149], v[238:241], v[34:49]
	v_mfma_f32_32x32x16_bf16 v[18:33], v[138:141], v[200:203], v[18:33]
	v_max_f32_e32 v238, v83, v83
	v_max_f32_e32 v239, v82, v82
	v_max_f32_e32 v238, v239, v238
	v_max3_f32 v238, v238, v84, v85
	v_max3_f32 v238, v238, v86, v87
	v_max3_f32 v138, v238, v88, v89
	v_max3_f32 v138, v138, v90, v91
	v_max3_f32 v138, v138, v92, v93
	v_mfma_f32_32x32x16_bf16 v[18:33], v[142:145], v[230:233], v[18:33]
	v_max3_f32 v138, v138, v94, v95
	v_max3_f32 v138, v138, v96, v97
	v_max3_f32 v138, v138, v66, v67
	v_max3_f32 v138, v138, v68, v69
	v_max3_f32 v138, v138, v70, v71
	v_max3_f32 v138, v138, v72, v73
	v_max3_f32 v138, v138, v74, v75
	v_max3_f32 v138, v138, v76, v77
	v_mfma_f32_32x32x16_bf16 v[18:33], v[150:153], v[234:237], v[18:33]
	v_max3_f32 v138, v138, v78, v79
	v_max3_f32 v138, v138, v80, v81
	v_mov_b32_e32 v139, v138
	s_nop 1
	v_permlane32_swap_b32_e32 v138, v139
	v_max_f32_e32 v139, v139, v139
	v_max_f32_e32 v138, v138, v138
	v_max_f32_e32 v138, v138, v139
	v_max_f32_e32 v140, v227, v227
	v_sub_f32_e32 v139, v138, v227
	v_max_f32_e32 v138, v140, v138
	v_mfma_f32_32x32x16_bf16 v[18:33], v[146:149], v[242:245], v[18:33]
	v_sub_f32_e32 v140, v227, v138
	v_mul_f32_e32 v140, 0x3e38aa3b, v140
	v_exp_f32_e32 v140, v140
	v_cmp_ge_f32_e32 vcc, s7, v139
	s_cmp_eq_u64 vcc, exec
	s_cselect_b64 s[4:5], -1, 0
	s_waitcnt vmcnt(3)
	ds_write_b128 v222, v[134:137] offset:49152
	s_waitcnt lgkmcnt(0)
	s_barrier
	s_waitcnt vmcnt(3)
	v_cndmask_b32_e64 v141, v140, 1.0, s[4:5]
	v_cmp_gt_f32_e32 vcc, 1.0, v141
	s_waitcnt vmcnt(3)
	ds_write_b128 v215, v[126:129] offset:16384
	s_waitcnt vmcnt(3)
	ds_write_b128 v216, v[130:133] offset:16384
	s_waitcnt vmcnt(3)
	s_cbranch_vccz .LBB0_422
	s_and_saveexec_b64 s[52:53], s[0:1]
	ds_write_b32 v171, v141 offset:128
	s_or_b64 exec, exec, s[52:53]
	s_waitcnt lgkmcnt(0)
	ds_read_b128 v[126:129], v207 offset:224
	ds_read_b128 v[130:133], v207 offset:192
	ds_read_b128 v[134:137], v207 offset:160
	ds_read_b128 v[142:145], v207 offset:128
	s_waitcnt lgkmcnt(3)
	v_pk_mul_f32 v[16:17], v[16:17], v[128:129]
	s_waitcnt lgkmcnt(2)
	v_pk_mul_f32 v[12:13], v[12:13], v[132:133]
	s_waitcnt lgkmcnt(1)
	v_pk_mul_f32 v[8:9], v[8:9], v[136:137]
	s_waitcnt lgkmcnt(0)
	v_pk_mul_f32 v[4:5], v[4:5], v[144:145]
	v_pk_mul_f32 v[14:15], v[14:15], v[126:127]
	v_pk_mul_f32 v[10:11], v[10:11], v[130:131]
	v_pk_mul_f32 v[6:7], v[6:7], v[134:135]
	v_pk_mul_f32 v[2:3], v[2:3], v[142:143]
	v_pk_mul_f32 v[64:65], v[64:65], v[128:129]
	v_pk_mul_f32 v[60:61], v[60:61], v[132:133]
	v_pk_mul_f32 v[56:57], v[56:57], v[136:137]
	v_pk_mul_f32 v[52:53], v[52:53], v[144:145]
	v_pk_mul_f32 v[62:63], v[62:63], v[126:127]
	v_pk_mul_f32 v[58:59], v[58:59], v[130:131]
	v_pk_mul_f32 v[54:55], v[54:55], v[134:135]
	v_pk_mul_f32 v[50:51], v[50:51], v[142:143]
	v_pk_mul_f32 v[48:49], v[48:49], v[128:129]
	v_pk_mul_f32 v[44:45], v[44:45], v[132:133]
	v_pk_mul_f32 v[40:41], v[40:41], v[136:137]
	v_pk_mul_f32 v[36:37], v[36:37], v[144:145]
	v_pk_mul_f32 v[46:47], v[46:47], v[126:127]
	v_pk_mul_f32 v[42:43], v[42:43], v[130:131]
	v_pk_mul_f32 v[38:39], v[38:39], v[134:135]
	v_pk_mul_f32 v[34:35], v[34:35], v[142:143]
	v_pk_mul_f32 v[32:33], v[32:33], v[128:129]
	v_pk_mul_f32 v[28:29], v[28:29], v[132:133]
	v_pk_mul_f32 v[24:25], v[24:25], v[136:137]
	v_pk_mul_f32 v[20:21], v[20:21], v[144:145]
	v_pk_mul_f32 v[30:31], v[30:31], v[126:127]
	v_pk_mul_f32 v[26:27], v[26:27], v[130:131]
	v_pk_mul_f32 v[22:23], v[22:23], v[134:135]
	v_pk_mul_f32 v[18:19], v[18:19], v[142:143]

; #define SBAR() __builtin_amdgcn_sched_barrier(0)
; #define SWAIT() do { if constexpr (MODE == 1) asm volatile("s_waitcnt vmcnt(3)" ::: "memory"); else asm volatile("s_waitcnt vmcnt(4)" ::: "memory"); } while (0)
; template <int MODE>
; __device__ __forceinline__ void attn_pass(const bf16_t* __restrict__ Qb, const bf16_t* __restrict__ Kh, const bf16_t* __restrict__ Vh, const int NT, const int kr0, const int g4, const int map,
;                                           LAS unsigned char* lds, f32x16 (&o)[4]) {
;     ...
;         if (j + 3 < NT) SLOAD(SE, j + 3); SBAR();
;         pv_d0(o, vb0 + SHM_V, pa0, pa1, pa2, pa3); partialSM<MODE>(pA0, pA1, m_reg, mnA, alA);
;         __syncthreads(); SWAIT(); SWRITE(1, SO);
.Lp3_drain_0:
	s_waitcnt vmcnt(0)
	s_branch .LBB0_418

; #define SWAIT() do { if constexpr (MODE == 1) asm volatile("s_waitcnt vmcnt(3)" ::: "memory"); else asm volatile("s_waitcnt vmcnt(4)" ::: "memory"); } while (0)
; #define RESC(a) do { if (__any((a) < 1.f)) { if (hi == 0) al_l[r32] = (a); asm volatile("s_waitcnt lgkmcnt(0)" ::: "memory"); \
;     _Pragma("unroll") for (int d = 0; d < 4; ++d) _Pragma("unroll") for (int r = 0; r < 16; ++r) o[d][r] *= al_l[crow(r, hi)]; } } while (0)
; template <int MODE>
; __device__ __forceinline__ void partialSM(f32x16& p0, f32x16& p1, float& m_reg, float& mn, float& alpha) {
;     constexpr float SCALE = Cfg<MODE>::SCALE, C = SCALE * 1.4426950408889634f;
;     float pmax = p0[0];
; #pragma unroll
;     for (int r = 1; r < 16; ++r) pmax = fmaxf(pmax, p0[r]);
; #pragma unroll
;     for (int r = 0; r < 16; ++r) pmax = fmaxf(pmax, p1[r]);
;     { auto rr = __builtin_amdgcn_permlane32_swap(__float_as_uint(pmax), __float_as_uint(pmax), false, false);
;       pmax = fmaxf(__uint_as_float(rr[0]), __uint_as_float(rr[1])); }
;     if (__builtin_expect(__all(pmax - m_reg <= THR / SCALE), 1)) { mn = m_reg; alpha = 1.f; }
;     else { mn = fmaxf(m_reg, pmax); alpha = __builtin_amdgcn_exp2f((m_reg - mn) * C); m_reg = mn; }
;     const float mnC = -mn * C;
; #pragma unroll
;     for (int r = 0; r < 16; ++r) p0[r] = fmaf(p0[r], C, mnC);
; #pragma unroll
;     for (int r = 0; r < 16; ++r) p1[r] = fmaf(p1[r], C, mnC);
; #pragma unroll
;     for (int r = 0; r < 16; ++r) p0[r] = __builtin_amdgcn_exp2f(p0[r]);
; }
; template <int MODE>
; __device__ __forceinline__ void attn_pass(const bf16_t* __restrict__ Qb, const bf16_t* __restrict__ Kh, const bf16_t* __restrict__ Vh, const int NT, const int kr0, const int g4, const int map,
;                                           LAS unsigned char* lds, f32x16 (&o)[4]) {
;     ...
;         pv_d0(o, vb0 + SHM_V, pa0, pa1, pa2, pa3); partialSM<MODE>(pA0, pA1, m_reg, mnA, alA);
;         __syncthreads(); SWAIT(); SWRITE(1, SO);
;         RESC(alA); __syncthreads();
.LBB0_437:
	ds_read_b64_tr_b16 v[166:167], v173 offset:0
	ds_read_b64_tr_b16 v[168:169], v173 offset:0x800
	ds_read_b64_tr_b16 v[218:219], v173 offset:0x1000
	ds_read_b64_tr_b16 v[220:221], v173 offset:0x1800
	ds_read_b64_tr_b16 v[222:223], v173 offset:0x2000
	ds_read_b64_tr_b16 v[224:225], v173 offset:0x2800
	ds_read_b64_tr_b16 v[226:227], v173 offset:0x3000
	ds_read_b64_tr_b16 v[228:229], v173 offset:0x3800
	s_waitcnt lgkmcnt(0)
	s_nop 0
	v_mfma_f32_32x32x16_bf16 v[2:17], v[138:141], v[166:169], v[2:17]
	ds_read_b64_tr_b16 v[166:167], v173 offset:0x200
	ds_read_b64_tr_b16 v[168:169], v173 offset:0xa00
	v_mfma_f32_32x32x16_bf16 v[2:17], v[142:145], v[218:221], v[2:17]
	ds_read_b64_tr_b16 v[218:219], v173 offset:0x1200
	ds_read_b64_tr_b16 v[220:221], v173 offset:0x1a00
	v_mfma_f32_32x32x16_bf16 v[2:17], v[150:153], v[222:225], v[2:17]
	ds_read_b64_tr_b16 v[222:223], v173 offset:0x2200
	ds_read_b64_tr_b16 v[224:225], v173 offset:0x2a00
	ds_read_b64_tr_b16 v[230:231], v173 offset:0x3200
	ds_read_b64_tr_b16 v[232:233], v173 offset:0x3a00
	s_waitcnt lgkmcnt(0)
	v_mfma_f32_32x32x16_bf16 v[2:17], v[146:149], v[226:229], v[2:17]
	v_mfma_f32_32x32x16_bf16 v[50:65], v[138:141], v[166:169], v[50:65]
	ds_read_b64_tr_b16 v[166:167], v173 offset:0x400
	ds_read_b64_tr_b16 v[168:169], v173 offset:0xc00
	v_mfma_f32_32x32x16_bf16 v[50:65], v[142:145], v[218:221], v[50:65]
	ds_read_b64_tr_b16 v[218:219], v173 offset:0x1400
	ds_read_b64_tr_b16 v[220:221], v173 offset:0x1c00
	v_mfma_f32_32x32x16_bf16 v[50:65], v[150:153], v[222:225], v[50:65]
	ds_read_b64_tr_b16 v[222:223], v173 offset:0x2400
	ds_read_b64_tr_b16 v[224:225], v173 offset:0x2c00
	ds_read_b64_tr_b16 v[226:227], v173 offset:0x3400
	ds_read_b64_tr_b16 v[228:229], v173 offset:0x3c00
	s_waitcnt lgkmcnt(0)
	v_mfma_f32_32x32x16_bf16 v[50:65], v[146:149], v[230:233], v[50:65]
	v_mfma_f32_32x32x16_bf16 v[34:49], v[138:141], v[166:169], v[34:49]
	ds_read_b64_tr_b16 v[166:167], v173 offset:0x600
	ds_read_b64_tr_b16 v[168:169], v173 offset:0xe00
	v_mfma_f32_32x32x16_bf16 v[34:49], v[142:145], v[218:221], v[34:49]
	ds_read_b64_tr_b16 v[218:219], v173 offset:0x1600
	ds_read_b64_tr_b16 v[220:221], v173 offset:0x1e00
	v_mfma_f32_32x32x16_bf16 v[34:49], v[150:153], v[222:225], v[34:49]
	ds_read_b64_tr_b16 v[222:223], v173 offset:0x2600
	ds_read_b64_tr_b16 v[224:225], v173 offset:0x2e00
	ds_read_b64_tr_b16 v[230:231], v173 offset:0x3600
	ds_read_b64_tr_b16 v[232:233], v173 offset:0x3e00
	s_waitcnt lgkmcnt(0)
	v_mfma_f32_32x32x16_bf16 v[34:49], v[146:149], v[226:229], v[34:49]
	v_mfma_f32_32x32x16_bf16 v[18:33], v[138:141], v[166:169], v[18:33]
	v_max_f32_e32 v191, v83, v83
	v_max_f32_e32 v192, v82, v82
	v_max_f32_e32 v191, v192, v191
	v_max3_f32 v191, v191, v84, v85
	v_max3_f32 v191, v191, v86, v87
	v_max3_f32 v138, v191, v88, v89
	v_max3_f32 v138, v138, v90, v91
	v_max3_f32 v138, v138, v92, v93
	v_mfma_f32_32x32x16_bf16 v[18:33], v[142:145], v[218:221], v[18:33]
	v_max3_f32 v138, v138, v94, v95
	v_max3_f32 v138, v138, v96, v97
	v_max3_f32 v138, v138, v66, v67
	v_max3_f32 v138, v138, v68, v69
	v_max3_f32 v138, v138, v70, v71
	v_max3_f32 v138, v138, v72, v73
	v_max3_f32 v138, v138, v74, v75
	v_max3_f32 v138, v138, v76, v77
	v_mfma_f32_32x32x16_bf16 v[18:33], v[150:153], v[222:225], v[18:33]
	v_max3_f32 v138, v138, v78, v79
	v_max3_f32 v138, v138, v80, v81
	v_mov_b32_e32 v139, v138
	s_nop 1
	v_permlane32_swap_b32_e32 v138, v139
	v_max_f32_e32 v139, v139, v139
	v_max_f32_e32 v138, v138, v138
	v_max_f32_e32 v138, v138, v139
	v_max_f32_e32 v140, v188, v188
	v_sub_f32_e32 v139, v138, v188
	v_max_f32_e32 v138, v140, v138
	v_mfma_f32_32x32x16_bf16 v[18:33], v[146:149], v[230:233], v[18:33]
	v_sub_f32_e32 v140, v188, v138
	v_mul_f32_e32 v140, 0x3e38aa3b, v140
	v_exp_f32_e32 v140, v140
	v_cmp_ge_f32_e32 vcc, s7, v139
	s_cmp_eq_u64 vcc, exec
	s_cselect_b64 s[4:5], -1, 0
	s_waitcnt vmcnt(3)
	ds_write_b128 v179, v[134:137] offset:49152
	s_waitcnt lgkmcnt(0)
	s_barrier
	s_waitcnt vmcnt(3)
	v_cndmask_b32_e64 v141, v140, 1.0, s[4:5]
	v_cmp_gt_f32_e32 vcc, 1.0, v141
	s_waitcnt vmcnt(3)
	ds_write_b128 v215, v[126:129] offset:16384
	s_waitcnt vmcnt(3)
	ds_write_b128 v216, v[130:133] offset:16384
	s_waitcnt vmcnt(3)
	s_cbranch_vccz .LBB0_441
	s_and_saveexec_b64 s[52:53], s[0:1]
	ds_write_b32 v171, v141 offset:128
	s_or_b64 exec, exec, s[52:53]
	s_waitcnt lgkmcnt(0)
	ds_read_b128 v[126:129], v207 offset:224
	ds_read_b128 v[130:133], v207 offset:192
	ds_read_b128 v[134:137], v207 offset:160
	ds_read_b128 v[142:145], v207 offset:128
	s_waitcnt lgkmcnt(3)
	v_pk_mul_f32 v[16:17], v[16:17], v[128:129]
	s_waitcnt lgkmcnt(2)
	v_pk_mul_f32 v[12:13], v[12:13], v[132:133]
	s_waitcnt lgkmcnt(1)
	v_pk_mul_f32 v[8:9], v[8:9], v[136:137]
	s_waitcnt lgkmcnt(0)
	v_pk_mul_f32 v[4:5], v[4:5], v[144:145]
	v_pk_mul_f32 v[14:15], v[14:15], v[126:127]
	v_pk_mul_f32 v[10:11], v[10:11], v[130:131]
	v_pk_mul_f32 v[6:7], v[6:7], v[134:135]
	v_pk_mul_f32 v[2:3], v[2:3], v[142:143]
	v_pk_mul_f32 v[64:65], v[64:65], v[128:129]
	v_pk_mul_f32 v[60:61], v[60:61], v[132:133]
	v_pk_mul_f32 v[56:57], v[56:57], v[136:137]
	v_pk_mul_f32 v[52:53], v[52:53], v[144:145]
	v_pk_mul_f32 v[62:63], v[62:63], v[126:127]
	v_pk_mul_f32 v[58:59], v[58:59], v[130:131]
	v_pk_mul_f32 v[54:55], v[54:55], v[134:135]
	v_pk_mul_f32 v[50:51], v[50:51], v[142:143]
	v_pk_mul_f32 v[48:49], v[48:49], v[128:129]
	v_pk_mul_f32 v[44:45], v[44:45], v[132:133]
	v_pk_mul_f32 v[40:41], v[40:41], v[136:137]
	v_pk_mul_f32 v[36:37], v[36:37], v[144:145]
	v_pk_mul_f32 v[46:47], v[46:47], v[126:127]
	v_pk_mul_f32 v[42:43], v[42:43], v[130:131]
	v_pk_mul_f32 v[38:39], v[38:39], v[134:135]
	v_pk_mul_f32 v[34:35], v[34:35], v[142:143]
	v_pk_mul_f32 v[32:33], v[32:33], v[128:129]
	v_pk_mul_f32 v[28:29], v[28:29], v[132:133]
	v_pk_mul_f32 v[24:25], v[24:25], v[136:137]
	v_pk_mul_f32 v[20:21], v[20:21], v[144:145]
	v_pk_mul_f32 v[30:31], v[30:31], v[126:127]
	v_pk_mul_f32 v[26:27], v[26:27], v[130:131]
	v_pk_mul_f32 v[22:23], v[22:23], v[134:135]
	v_pk_mul_f32 v[18:19], v[18:19], v[142:143]

; #define SBAR() __builtin_amdgcn_sched_barrier(0)
; #define SWAIT() do { if constexpr (MODE == 1) asm volatile("s_waitcnt vmcnt(3)" ::: "memory"); else asm volatile("s_waitcnt vmcnt(4)" ::: "memory"); } while (0)
; template <int D0> __device__ __forceinline__ void pv_one(f32x16& od, int vb, bf16x8 pa0, bf16x8 pa1, bf16x8 pa2, bf16x8 pa3) {
;     const s16x4 l0 = tr_read<v_rd_off(D0, 0, 0)>(vb), h0 = tr_read<v_rd_off(D0, 0, 1)>(vb), l1 = tr_read<v_rd_off(D0, 1, 0)>(vb), h1 = tr_read<v_rd_off(D0, 1, 1)>(vb);
;     const s16x4 l2 = tr_read<v_rd_off(D0, 2, 0)>(vb), h2 = tr_read<v_rd_off(D0, 2, 1)>(vb), l3 = tr_read<v_rd_off(D0, 3, 0)>(vb), h3 = tr_read<v_rd_off(D0, 3, 1)>(vb);
;     asm volatile("s_waitcnt lgkmcnt(0)" ::: "memory"); SBAR();
;     ...
;     od = __builtin_amdgcn_mfma_f32_32x32x16_bf16(pa0, PKV(l0, h0), od, 0, 0, 0);
;     od = __builtin_amdgcn_mfma_f32_32x32x16_bf16(pa1, PKV(l1, h1), od, 0, 0, 0);
;     od = __builtin_amdgcn_mfma_f32_32x32x16_bf16(pa2, PKV(l2, h2), od, 0, 0, 0);
;     od = __builtin_amdgcn_mfma_f32_32x32x16_bf16(pa3, PKV(l3, h3), od, 0, 0, 0);
;     ...
; }
; __device__ __forceinline__ void pv_d0(f32x16* o, int vb, bf16x8 pa0, bf16x8 pa1, bf16x8 pa2, bf16x8 pa3) {
;     pv_one<0>(o[0], vb, pa0, pa1, pa2, pa3); pv_one<1>(o[1], vb, pa0, pa1, pa2, pa3); pv_one<2>(o[2], vb, pa0, pa1, pa2, pa3); pv_one<3>(o[3], vb, pa0, pa1, pa2, pa3);
; template <int MODE>
; __device__ __forceinline__ void attn_pass(const bf16_t* __restrict__ Qb, const bf16_t* __restrict__ Kh, const bf16_t* __restrict__ Vh, const int NT, const int kr0, const int g4, const int map,
;                                           LAS unsigned char* lds, f32x16 (&o)[4]) {
;     ...
;         pv_d0(o, vb0, pa0, pa1, pa2, pa3); partialSM<MODE>(pB0, pB1, m_reg, mnB, alB);
;         __syncthreads(); SWAIT(); SWRITE(0, SE);
;         RESC(alB); __syncthreads();
;         SBAR(); qkt<MODE>(pA0, pA1, K_lds, qr, Qs, r32, hi, cbase); MASK(pA0, pA1, j + 1);
;         finishSM(pB0, pB1, alB, l_reg, pa0, pa1, pa2, pa3); SBAR();
;         if (j + 3 < NT) SLOAD(SE, j + 3); SBAR();
;         pv_d0(o, vb0 + SHM_V, pa0, pa1, pa2, pa3); partialSM<MODE>(pA0, pA1, m_reg, mnA, alA);
;         __syncthreads(); SWAIT(); SWRITE(1, SO);
;         RESC(alA); __syncthreads();
.LBB0_477:
	ds_read_b64_tr_b16 v[228:229], v173 offset:0
	ds_read_b64_tr_b16 v[230:231], v173 offset:0x800
	ds_read_b64_tr_b16 v[232:233], v173 offset:0x1000
	ds_read_b64_tr_b16 v[234:235], v173 offset:0x1800
	ds_read_b64_tr_b16 v[236:237], v173 offset:0x2000
	ds_read_b64_tr_b16 v[238:239], v173 offset:0x2800
	ds_read_b64_tr_b16 v[240:241], v173 offset:0x3000
	ds_read_b64_tr_b16 v[242:243], v173 offset:0x3800
	s_waitcnt lgkmcnt(0)
	s_nop 0
	v_mfma_f32_32x32x16_bf16 v[2:17], v[68:71], v[228:231], v[2:17]
	ds_read_b64_tr_b16 v[228:229], v173 offset:0x200
	ds_read_b64_tr_b16 v[230:231], v173 offset:0xa00
	v_mfma_f32_32x32x16_bf16 v[2:17], v[76:79], v[232:235], v[2:17]
	ds_read_b64_tr_b16 v[232:233], v173 offset:0x1200
	ds_read_b64_tr_b16 v[234:235], v173 offset:0x1a00
	v_mfma_f32_32x32x16_bf16 v[2:17], v[166:169], v[236:239], v[2:17]
	ds_read_b64_tr_b16 v[236:237], v173 offset:0x2200
	ds_read_b64_tr_b16 v[238:239], v173 offset:0x2a00
	ds_read_b64_tr_b16 v[244:245], v173 offset:0x3200
	ds_read_b64_tr_b16 v[246:247], v173 offset:0x3a00
	s_waitcnt lgkmcnt(0)
	v_mfma_f32_32x32x16_bf16 v[2:17], v[162:165], v[240:243], v[2:17]
	v_mfma_f32_32x32x16_bf16 v[50:65], v[68:71], v[228:231], v[50:65]
	ds_read_b64_tr_b16 v[228:229], v173 offset:0x400
	ds_read_b64_tr_b16 v[230:231], v173 offset:0xc00
	v_mfma_f32_32x32x16_bf16 v[50:65], v[76:79], v[232:235], v[50:65]
	ds_read_b64_tr_b16 v[232:233], v173 offset:0x1400
	ds_read_b64_tr_b16 v[234:235], v173 offset:0x1c00
	v_mfma_f32_32x32x16_bf16 v[50:65], v[166:169], v[236:239], v[50:65]
	ds_read_b64_tr_b16 v[236:237], v173 offset:0x2400
	ds_read_b64_tr_b16 v[238:239], v173 offset:0x2c00
	ds_read_b64_tr_b16 v[240:241], v173 offset:0x3400
	ds_read_b64_tr_b16 v[242:243], v173 offset:0x3c00
	s_waitcnt lgkmcnt(0)
	v_mfma_f32_32x32x16_bf16 v[50:65], v[162:165], v[244:247], v[50:65]
	v_mfma_f32_32x32x16_bf16 v[34:49], v[68:71], v[228:231], v[34:49]
	ds_read_b64_tr_b16 v[228:229], v173 offset:0x600
	ds_read_b64_tr_b16 v[230:231], v173 offset:0xe00
	v_mfma_f32_32x32x16_bf16 v[34:49], v[76:79], v[232:235], v[34:49]
	ds_read_b64_tr_b16 v[232:233], v173 offset:0x1600
	ds_read_b64_tr_b16 v[234:235], v173 offset:0x1e00
	v_mfma_f32_32x32x16_bf16 v[34:49], v[166:169], v[236:239], v[34:49]
	ds_read_b64_tr_b16 v[236:237], v173 offset:0x2600
	ds_read_b64_tr_b16 v[238:239], v173 offset:0x2e00
	ds_read_b64_tr_b16 v[244:245], v173 offset:0x3600
	ds_read_b64_tr_b16 v[246:247], v173 offset:0x3e00
	s_waitcnt lgkmcnt(0)
	v_mfma_f32_32x32x16_bf16 v[34:49], v[162:165], v[240:243], v[34:49]
	v_mfma_f32_32x32x16_bf16 v[18:33], v[68:71], v[228:231], v[18:33]
	v_max_f32_e32 v75, v83, v83
	v_max_f32_e32 v80, v82, v82
	v_max_f32_e32 v75, v80, v75
	v_max3_f32 v75, v75, v84, v85
	v_max3_f32 v75, v75, v86, v87
	v_max3_f32 v68, v75, v88, v89
	v_max3_f32 v68, v68, v90, v91
	v_max3_f32 v68, v68, v92, v93
	v_mfma_f32_32x32x16_bf16 v[18:33], v[76:79], v[232:235], v[18:33]
	v_max3_f32 v68, v68, v94, v95
	v_max3_f32 v68, v68, v96, v97
	v_max3_f32 v66, v68, v66, v99
	v_max3_f32 v66, v66, v100, v101
	v_max3_f32 v66, v66, v102, v103
	v_max3_f32 v66, v66, v104, v73
	v_max3_f32 v66, v66, v74, v107
	v_max3_f32 v66, v66, v108, v109
	v_mfma_f32_32x32x16_bf16 v[18:33], v[166:169], v[236:239], v[18:33]
	v_max3_f32 v66, v66, v110, v111
	v_max3_f32 v66, v66, v112, v81
	v_mov_b32_e32 v68, v66
	s_nop 1
	v_permlane32_swap_b32_e32 v66, v68
	v_max_f32_e32 v68, v68, v68
	v_max_f32_e32 v66, v66, v66
	v_max_f32_e32 v66, v66, v68
	v_max_f32_e32 v69, v226, v226
	v_sub_f32_e32 v68, v66, v226
	v_max_f32_e32 v66, v69, v66
	v_mfma_f32_32x32x16_bf16 v[18:33], v[162:165], v[244:247], v[18:33]
	v_sub_f32_e32 v69, v226, v66
	v_mul_f32_e32 v69, 0x3e0293ee, v69
	v_exp_f32_e32 v69, v69
	v_cmp_ge_f32_e32 vcc, s7, v68
	s_cmp_eq_u64 vcc, exec
	s_cselect_b64 s[4:5], -1, 0
	s_waitcnt vmcnt(4)
	ds_write_b128 v192, v[154:157] offset:49152
	ds_write_b128 v193, v[158:161] offset:49152
	s_waitcnt lgkmcnt(0)
	s_barrier
	s_waitcnt vmcnt(4)
	v_cndmask_b32_e64 v98, v69, 1.0, s[4:5]
	v_cmp_gt_f32_e32 vcc, 1.0, v98
	s_waitcnt vmcnt(4)
	ds_write_b128 v199, v[146:149] offset:16384
	s_waitcnt vmcnt(4)
	ds_write_b128 v200, v[150:153] offset:16384
	s_waitcnt vmcnt(4)
	s_waitcnt vmcnt(4)
	s_cbranch_vccz .LBB0_481
	s_and_saveexec_b64 s[44:45], s[0:1]
	ds_write_b32 v171, v98 offset:128
	s_or_b64 exec, exec, s[44:45]
	s_waitcnt lgkmcnt(0)
	ds_read_b128 v[68:71], v207 offset:224
	ds_read_b128 v[74:77], v207 offset:192
	ds_read_b128 v[100:103], v207 offset:160
	ds_read_b128 v[104:107], v207 offset:128
	s_waitcnt lgkmcnt(3)
	v_pk_mul_f32 v[16:17], v[16:17], v[70:71]
	s_waitcnt lgkmcnt(2)
	v_pk_mul_f32 v[12:13], v[12:13], v[76:77]
	s_waitcnt lgkmcnt(1)
	v_pk_mul_f32 v[8:9], v[8:9], v[102:103]
	s_waitcnt lgkmcnt(0)
	v_pk_mul_f32 v[4:5], v[4:5], v[106:107]
	v_pk_mul_f32 v[14:15], v[14:15], v[68:69]
	v_pk_mul_f32 v[10:11], v[10:11], v[74:75]
	v_pk_mul_f32 v[6:7], v[6:7], v[100:101]
	v_pk_mul_f32 v[2:3], v[2:3], v[104:105]
	v_pk_mul_f32 v[64:65], v[64:65], v[70:71]
	v_pk_mul_f32 v[60:61], v[60:61], v[76:77]
	v_pk_mul_f32 v[56:57], v[56:57], v[102:103]
	v_pk_mul_f32 v[52:53], v[52:53], v[106:107]
	v_pk_mul_f32 v[62:63], v[62:63], v[68:69]
	v_pk_mul_f32 v[58:59], v[58:59], v[74:75]
	v_pk_mul_f32 v[54:55], v[54:55], v[100:101]
	v_pk_mul_f32 v[50:51], v[50:51], v[104:105]
	v_pk_mul_f32 v[48:49], v[48:49], v[70:71]
	v_pk_mul_f32 v[44:45], v[44:45], v[76:77]
	v_pk_mul_f32 v[40:41], v[40:41], v[102:103]
	v_pk_mul_f32 v[36:37], v[36:37], v[106:107]
	v_pk_mul_f32 v[46:47], v[46:47], v[68:69]
	v_pk_mul_f32 v[42:43], v[42:43], v[74:75]
	v_pk_mul_f32 v[38:39], v[38:39], v[100:101]
	v_pk_mul_f32 v[34:35], v[34:35], v[104:105]
	v_pk_mul_f32 v[32:33], v[32:33], v[70:71]
	v_pk_mul_f32 v[28:29], v[28:29], v[76:77]
	v_pk_mul_f32 v[24:25], v[24:25], v[102:103]
	v_pk_mul_f32 v[20:21], v[20:21], v[106:107]
	v_pk_mul_f32 v[30:31], v[30:31], v[68:69]
	v_pk_mul_f32 v[26:27], v[26:27], v[74:75]
	v_pk_mul_f32 v[22:23], v[22:23], v[100:101]
	v_pk_mul_f32 v[18:19], v[18:19], v[104:105]
